# memory-K head norm (layer 0): the wave's 8 rows loaded up front instead of 8 serial load-reduce-store trips
# speedup vs baseline: 1.0162x; 1.0162x over previous
; __device__ __forceinline__ unsigned pk_bf16(float lo, float hi) { f32x2 v = {lo, hi}; bf16x2_t b = __builtin_convertvector(v, bf16x2_t); return __builtin_bit_cast(unsigned, b); }
; __device__ __forceinline__ float bf_lo(unsigned w) { return __uint_as_float(w << 16); }
; __device__ __forceinline__ float bf_hi(unsigned w) { return __uint_as_float(w & 0xffff0000u); }
; __device__ __forceinline__ void phase_kxnorm(const Frame& F, const Params& P) {
;     const int gw = F.bid * NWAVES + F.wave, NGW = F.G * NWAVES, lane = F.lane;
;     for (int it = gw; it < 2 * B * MEM * XH; it += NGW) { const int h = it & 3, row = (it >> 2) & (B * MEM - 1), l = it >> 13;
;         bf16_t* p = (bf16_t*)(F.ws + WS_KXV) + ((size_t)l * B * MEM + row) * 1024 + h * XHD + 2 * lane; const unsigned w = *(const unsigned*)p;
;         const float a = bf_lo(w), b = bf_hi(w); const float ss = wave_sum(a * a + b * b); const float r = __builtin_amdgcn_rsqf(ss * (1.0f / XHD) + EPS); const float* g = P.in[21] + l * XHD + 2 * lane;
;         *(unsigned*)p = pk_bf16(a * r * g[0], b * r * g[1]); }
; }
.LBB0_572:
	s_cmp_lg_u32 s20, 0
	v_readlane_b32 s2, v255, 4
	s_cselect_b64 s[0:1], -1, 0
	v_readlane_b32 s3, v255, 5
	s_or_b64 s[0:1], s[2:3], s[0:1]
	s_and_b64 vcc, exec, s[0:1]
	s_cbranch_vccnz .LBB0_575
	v_and_b32_e32 v0, 64, v251
	v_add_u32_e32 v0, 64, v0
	v_xor_b32_e32 v1, 1, v251
	v_cmp_lt_i32_e32 vcc, v1, v0
	v_readlane_b32 s0, v255, 26
	v_readlane_b32 s4, v253, 37
	v_cndmask_b32_e32 v1, v251, v1, vcc
	v_lshlrev_b32_e32 v2, 2, v1
	v_xor_b32_e32 v1, 2, v251
	v_cmp_lt_i32_e32 vcc, v1, v0
	v_readlane_b32 s1, v255, 27
	s_add_u32 s0, s0, 0x700000
	v_cndmask_b32_e32 v1, v251, v1, vcc
	v_lshlrev_b32_e32 v3, 2, v1
	v_xor_b32_e32 v1, 4, v251
	v_cmp_lt_i32_e32 vcc, v1, v0
	v_lshlrev_b32_e32 v8, 1, v165
	v_lshlrev_b32_e32 v112, 3, v165
	v_cndmask_b32_e32 v1, v251, v1, vcc
	v_lshlrev_b32_e32 v4, 2, v1
	v_xor_b32_e32 v1, 8, v251
	v_cmp_lt_i32_e32 vcc, v1, v0
	v_readlane_b32 s5, v253, 38
	v_readlane_b32 s14, v253, 47
	v_cndmask_b32_e32 v1, v251, v1, vcc
	v_lshlrev_b32_e32 v5, 2, v1
	v_xor_b32_e32 v1, 16, v251
	v_cmp_lt_i32_e32 vcc, v1, v0
	v_readlane_b32 s15, v253, 48
	s_addc_u32 s1, s1, 0
	v_cndmask_b32_e32 v1, v251, v1, vcc
	v_lshlrev_b32_e32 v6, 2, v1
	v_xor_b32_e32 v1, 32, v251
	v_cmp_lt_i32_e32 vcc, v1, v0
	v_readlane_b32 s2, v254, 43
	v_readlane_b32 s3, v254, 42
	v_cndmask_b32_e32 v0, v251, v1, vcc
	v_lshlrev_b32_e32 v7, 2, v0
	v_lshl_add_u64 v[0:1], s[14:15], 0, v[112:113]
	v_lshlrev_b32_e32 v112, 1, v8
	v_readlane_b32 s4, v255, 0
	v_readlane_b32 s6, v253, 39
	v_readlane_b32 s7, v253, 40
	v_readlane_b32 s8, v253, 41
	v_readlane_b32 s9, v253, 42
	v_readlane_b32 s10, v253, 43
	v_readlane_b32 s11, v253, 44
	v_readlane_b32 s12, v253, 45
	v_readlane_b32 s13, v253, 46
	v_readlane_b32 s16, v253, 49
	v_readlane_b32 s17, v253, 50
	v_readlane_b32 s18, v253, 51
	v_readlane_b32 s19, v253, 52
	v_readlane_b32 s5, v255, 1
	s_cmpk_lg_i32 s76, 0x800
	s_cbranch_scc1 .Lkx_orig
	s_ashr_i32 s6, s4, 13
	s_ashr_i32 s7, s6, 31
	s_and_b32 s5, s2, 0x1ffc00
	s_lshl_b64 s[8:9], s[6:7], 22
	s_add_u32 s7, s0, s8
	s_addc_u32 s8, s1, s9
	s_lshl_b32 s5, s5, 1
	s_add_u32 s5, s7, s5
	s_addc_u32 s7, s8, 0
	s_and_b32 s8, s3, 0x180
	s_lshl_b32 s8, s8, 1
	s_add_u32 s8, s5, s8
	s_addc_u32 s9, s7, 0
	v_lshl_add_u64 v[218:219], s[8:9], 0, v[112:113]
	s_mov_b64 s[6:7], 0x100000
	global_load_dwordx2 v[220:221], v[0:1], off
	global_load_dwordx2 v[222:223], v[0:1], off offset:512
	v_mov_b32_e32 v8, v218
	v_mov_b32_e32 v9, v219
	global_load_dword v224, v[8:9], off
	v_lshl_add_u64 v[8:9], v[8:9], 0, s[6:7]
	global_load_dword v225, v[8:9], off
	v_lshl_add_u64 v[8:9], v[8:9], 0, s[6:7]
	global_load_dword v226, v[8:9], off
	v_lshl_add_u64 v[8:9], v[8:9], 0, s[6:7]
	global_load_dword v227, v[8:9], off
	v_lshl_add_u64 v[8:9], v[8:9], 0, s[6:7]
	global_load_dword v228, v[8:9], off
	v_lshl_add_u64 v[8:9], v[8:9], 0, s[6:7]
	global_load_dword v229, v[8:9], off
	v_lshl_add_u64 v[8:9], v[8:9], 0, s[6:7]
	global_load_dword v230, v[8:9], off
	v_lshl_add_u64 v[8:9], v[8:9], 0, s[6:7]
	global_load_dword v231, v[8:9], off
	v_lshl_add_u64 v[8:9], v[8:9], 0, s[6:7]
	v_mov_b32_e32 v8, v218
	v_mov_b32_e32 v9, v219
	s_waitcnt vmcnt(7)
	v_lshlrev_b32_e32 v12, 16, v224
	v_and_b32_e32 v13, 0xffff0000, v224
	v_pk_mul_f32 v[14:15], v[12:13], v[12:13]
	s_nop 0
	v_add_f32_e32 v14, v14, v15
	s_nop 1
	v_add_f32_dpp v15, v14, v14 quad_perm:[1,0,3,2] row_mask:0xf bank_mask:0xf
	s_nop 1
	v_add_f32_dpp v14, v15, v15 quad_perm:[2,3,0,1] row_mask:0xf bank_mask:0xf
	s_nop 1
	v_add_f32_dpp v15, v14, v14 row_half_mirror row_mask:0xf bank_mask:0xf
	s_nop 1
	v_add_f32_dpp v14, v15, v15 row_mirror row_mask:0xf bank_mask:0xf
	v_mov_b32_e32 v15, v14
	s_nop 1
	v_permlane16_swap_b32_e32 v14, v15
	v_add_f32_e32 v14, v14, v15
	v_mov_b32_e32 v15, v14
	s_nop 1
	v_permlane32_swap_b32_e32 v14, v15
	v_add_f32_e32 v14, v14, v15
	v_fmamk_f32 v14, v14, 0x3c000000, v249
	v_rsq_f32_e32 v14, v14
	s_nop 0
	v_pk_mul_f32 v[12:13], v[14:15], v[12:13] op_sel_hi:[0,1]
	v_pk_mul_f32 v[10:11], v[220:221], v[12:13]
	s_nop 0
	v_cvt_pk_bf16_f32 v10, v10, v11
	global_store_dword v[8:9], v10, off
	v_lshl_add_u64 v[8:9], v[8:9], 0, s[6:7]
	s_waitcnt vmcnt(7)
	v_lshlrev_b32_e32 v12, 16, v225
	v_and_b32_e32 v13, 0xffff0000, v225
	v_pk_mul_f32 v[14:15], v[12:13], v[12:13]
	s_nop 0
	v_add_f32_e32 v14, v14, v15
	s_nop 1
	v_add_f32_dpp v15, v14, v14 quad_perm:[1,0,3,2] row_mask:0xf bank_mask:0xf
	s_nop 1
	v_add_f32_dpp v14, v15, v15 quad_perm:[2,3,0,1] row_mask:0xf bank_mask:0xf
	s_nop 1
	v_add_f32_dpp v15, v14, v14 row_half_mirror row_mask:0xf bank_mask:0xf
	s_nop 1
	v_add_f32_dpp v14, v15, v15 row_mirror row_mask:0xf bank_mask:0xf
	v_mov_b32_e32 v15, v14
	s_nop 1
	v_permlane16_swap_b32_e32 v14, v15
	v_add_f32_e32 v14, v14, v15
	v_mov_b32_e32 v15, v14
	s_nop 1
	v_permlane32_swap_b32_e32 v14, v15
	v_add_f32_e32 v14, v14, v15
	v_fmamk_f32 v14, v14, 0x3c000000, v249
	v_rsq_f32_e32 v14, v14
	s_nop 0
	v_pk_mul_f32 v[12:13], v[14:15], v[12:13] op_sel_hi:[0,1]
	v_pk_mul_f32 v[10:11], v[220:221], v[12:13]
	s_nop 0
	v_cvt_pk_bf16_f32 v10, v10, v11
	global_store_dword v[8:9], v10, off
	v_lshl_add_u64 v[8:9], v[8:9], 0, s[6:7]
	s_waitcnt vmcnt(7)
	v_lshlrev_b32_e32 v12, 16, v226
	v_and_b32_e32 v13, 0xffff0000, v226
	v_pk_mul_f32 v[14:15], v[12:13], v[12:13]
	s_nop 0
	v_add_f32_e32 v14, v14, v15
	s_nop 1
	v_add_f32_dpp v15, v14, v14 quad_perm:[1,0,3,2] row_mask:0xf bank_mask:0xf
	s_nop 1
	v_add_f32_dpp v14, v15, v15 quad_perm:[2,3,0,1] row_mask:0xf bank_mask:0xf
	s_nop 1
	v_add_f32_dpp v15, v14, v14 row_half_mirror row_mask:0xf bank_mask:0xf
	s_nop 1
	v_add_f32_dpp v14, v15, v15 row_mirror row_mask:0xf bank_mask:0xf
	v_mov_b32_e32 v15, v14
	s_nop 1
	v_permlane16_swap_b32_e32 v14, v15
	v_add_f32_e32 v14, v14, v15
	v_mov_b32_e32 v15, v14
	s_nop 1
	v_permlane32_swap_b32_e32 v14, v15
	v_add_f32_e32 v14, v14, v15
	v_fmamk_f32 v14, v14, 0x3c000000, v249
	v_rsq_f32_e32 v14, v14
	s_nop 0
	v_pk_mul_f32 v[12:13], v[14:15], v[12:13] op_sel_hi:[0,1]
	v_pk_mul_f32 v[10:11], v[220:221], v[12:13]
	s_nop 0
	v_cvt_pk_bf16_f32 v10, v10, v11
	global_store_dword v[8:9], v10, off
	v_lshl_add_u64 v[8:9], v[8:9], 0, s[6:7]
	s_waitcnt vmcnt(7)
; __device__ __forceinline__ unsigned pk_bf16(float lo, float hi) { f32x2 v = {lo, hi}; bf16x2_t b = __builtin_convertvector(v, bf16x2_t); return __builtin_bit_cast(unsigned, b); }
; __device__ __forceinline__ float bf_lo(unsigned w) { return __uint_as_float(w << 16); }
; __device__ __forceinline__ float bf_hi(unsigned w) { return __uint_as_float(w & 0xffff0000u); }
; __device__ __forceinline__ void phase_kxnorm(const Frame& F, const Params& P) {
;     const int gw = F.bid * NWAVES + F.wave, NGW = F.G * NWAVES, lane = F.lane;
;     for (int it = gw; it < 2 * B * MEM * XH; it += NGW) { const int h = it & 3, row = (it >> 2) & (B * MEM - 1), l = it >> 13;
;         bf16_t* p = (bf16_t*)(F.ws + WS_KXV) + ((size_t)l * B * MEM + row) * 1024 + h * XHD + 2 * lane; const unsigned w = *(const unsigned*)p;
;         const float a = bf_lo(w), b = bf_hi(w); const float ss = wave_sum(a * a + b * b); const float r = __builtin_amdgcn_rsqf(ss * (1.0f / XHD) + EPS); const float* g = P.in[21] + l * XHD + 2 * lane;
;         *(unsigned*)p = pk_bf16(a * r * g[0], b * r * g[1]); }
; }
	v_lshlrev_b32_e32 v12, 16, v227
	v_and_b32_e32 v13, 0xffff0000, v227
	v_pk_mul_f32 v[14:15], v[12:13], v[12:13]
	s_nop 0
	v_add_f32_e32 v14, v14, v15
	s_nop 1
	v_add_f32_dpp v15, v14, v14 quad_perm:[1,0,3,2] row_mask:0xf bank_mask:0xf
	s_nop 1
	v_add_f32_dpp v14, v15, v15 quad_perm:[2,3,0,1] row_mask:0xf bank_mask:0xf
	s_nop 1
	v_add_f32_dpp v15, v14, v14 row_half_mirror row_mask:0xf bank_mask:0xf
	s_nop 1
	v_add_f32_dpp v14, v15, v15 row_mirror row_mask:0xf bank_mask:0xf
	v_mov_b32_e32 v15, v14
	s_nop 1
	v_permlane16_swap_b32_e32 v14, v15
	v_add_f32_e32 v14, v14, v15
	v_mov_b32_e32 v15, v14
	s_nop 1
	v_permlane32_swap_b32_e32 v14, v15
	v_add_f32_e32 v14, v14, v15
	v_fmamk_f32 v14, v14, 0x3c000000, v249
	v_rsq_f32_e32 v14, v14
	s_nop 0
	v_pk_mul_f32 v[12:13], v[14:15], v[12:13] op_sel_hi:[0,1]
	v_pk_mul_f32 v[10:11], v[220:221], v[12:13]
	s_nop 0
	v_cvt_pk_bf16_f32 v10, v10, v11
	global_store_dword v[8:9], v10, off
	v_lshl_add_u64 v[8:9], v[8:9], 0, s[6:7]
	s_waitcnt vmcnt(7)
	v_lshlrev_b32_e32 v12, 16, v228
	v_and_b32_e32 v13, 0xffff0000, v228
	v_pk_mul_f32 v[14:15], v[12:13], v[12:13]
	s_nop 0
	v_add_f32_e32 v14, v14, v15
	s_nop 1
	v_add_f32_dpp v15, v14, v14 quad_perm:[1,0,3,2] row_mask:0xf bank_mask:0xf
	s_nop 1
	v_add_f32_dpp v14, v15, v15 quad_perm:[2,3,0,1] row_mask:0xf bank_mask:0xf
	s_nop 1
	v_add_f32_dpp v15, v14, v14 row_half_mirror row_mask:0xf bank_mask:0xf
	s_nop 1
	v_add_f32_dpp v14, v15, v15 row_mirror row_mask:0xf bank_mask:0xf
	v_mov_b32_e32 v15, v14
	s_nop 1
	v_permlane16_swap_b32_e32 v14, v15
	v_add_f32_e32 v14, v14, v15
	v_mov_b32_e32 v15, v14
	s_nop 1
	v_permlane32_swap_b32_e32 v14, v15
	v_add_f32_e32 v14, v14, v15
	v_fmamk_f32 v14, v14, 0x3c000000, v249
	v_rsq_f32_e32 v14, v14
	s_nop 0
	v_pk_mul_f32 v[12:13], v[14:15], v[12:13] op_sel_hi:[0,1]
	v_pk_mul_f32 v[10:11], v[222:223], v[12:13]
	s_nop 0
	v_cvt_pk_bf16_f32 v10, v10, v11
	global_store_dword v[8:9], v10, off
	v_lshl_add_u64 v[8:9], v[8:9], 0, s[6:7]
	s_waitcnt vmcnt(7)
	v_lshlrev_b32_e32 v12, 16, v229
	v_and_b32_e32 v13, 0xffff0000, v229
	v_pk_mul_f32 v[14:15], v[12:13], v[12:13]
	s_nop 0
	v_add_f32_e32 v14, v14, v15
	s_nop 1
	v_add_f32_dpp v15, v14, v14 quad_perm:[1,0,3,2] row_mask:0xf bank_mask:0xf
	s_nop 1
	v_add_f32_dpp v14, v15, v15 quad_perm:[2,3,0,1] row_mask:0xf bank_mask:0xf
	s_nop 1
	v_add_f32_dpp v15, v14, v14 row_half_mirror row_mask:0xf bank_mask:0xf
	s_nop 1
	v_add_f32_dpp v14, v15, v15 row_mirror row_mask:0xf bank_mask:0xf
	v_mov_b32_e32 v15, v14
	s_nop 1
	v_permlane16_swap_b32_e32 v14, v15
	v_add_f32_e32 v14, v14, v15
	v_mov_b32_e32 v15, v14
	s_nop 1
	v_permlane32_swap_b32_e32 v14, v15
	v_add_f32_e32 v14, v14, v15
	v_fmamk_f32 v14, v14, 0x3c000000, v249
	v_rsq_f32_e32 v14, v14
	s_nop 0
	v_pk_mul_f32 v[12:13], v[14:15], v[12:13] op_sel_hi:[0,1]
	v_pk_mul_f32 v[10:11], v[222:223], v[12:13]
	s_nop 0
	v_cvt_pk_bf16_f32 v10, v10, v11
	global_store_dword v[8:9], v10, off
	v_lshl_add_u64 v[8:9], v[8:9], 0, s[6:7]
	s_waitcnt vmcnt(7)
	v_lshlrev_b32_e32 v12, 16, v230
	v_and_b32_e32 v13, 0xffff0000, v230
	v_pk_mul_f32 v[14:15], v[12:13], v[12:13]
	s_nop 0
	v_add_f32_e32 v14, v14, v15
	s_nop 1
	v_add_f32_dpp v15, v14, v14 quad_perm:[1,0,3,2] row_mask:0xf bank_mask:0xf
	s_nop 1
	v_add_f32_dpp v14, v15, v15 quad_perm:[2,3,0,1] row_mask:0xf bank_mask:0xf
	s_nop 1
	v_add_f32_dpp v15, v14, v14 row_half_mirror row_mask:0xf bank_mask:0xf
	s_nop 1
	v_add_f32_dpp v14, v15, v15 row_mirror row_mask:0xf bank_mask:0xf
	v_mov_b32_e32 v15, v14
	s_nop 1
	v_permlane16_swap_b32_e32 v14, v15
	v_add_f32_e32 v14, v14, v15
	v_mov_b32_e32 v15, v14
	s_nop 1
	v_permlane32_swap_b32_e32 v14, v15
	v_add_f32_e32 v14, v14, v15
	v_fmamk_f32 v14, v14, 0x3c000000, v249
	v_rsq_f32_e32 v14, v14
	s_nop 0
	v_pk_mul_f32 v[12:13], v[14:15], v[12:13] op_sel_hi:[0,1]
	v_pk_mul_f32 v[10:11], v[222:223], v[12:13]
	s_nop 0
	v_cvt_pk_bf16_f32 v10, v10, v11
	global_store_dword v[8:9], v10, off
	v_lshl_add_u64 v[8:9], v[8:9], 0, s[6:7]
	s_waitcnt vmcnt(7)
	v_lshlrev_b32_e32 v12, 16, v231
	v_and_b32_e32 v13, 0xffff0000, v231
	v_pk_mul_f32 v[14:15], v[12:13], v[12:13]
	s_nop 0
	v_add_f32_e32 v14, v14, v15
	s_nop 1
	v_add_f32_dpp v15, v14, v14 quad_perm:[1,0,3,2] row_mask:0xf bank_mask:0xf
	s_nop 1
	v_add_f32_dpp v14, v15, v15 quad_perm:[2,3,0,1] row_mask:0xf bank_mask:0xf
	s_nop 1
	v_add_f32_dpp v15, v14, v14 row_half_mirror row_mask:0xf bank_mask:0xf
	s_nop 1
	v_add_f32_dpp v14, v15, v15 row_mirror row_mask:0xf bank_mask:0xf
	v_mov_b32_e32 v15, v14
	s_nop 1
	v_permlane16_swap_b32_e32 v14, v15
	v_add_f32_e32 v14, v14, v15
	v_mov_b32_e32 v15, v14
	s_nop 1
	v_permlane32_swap_b32_e32 v14, v15
	v_add_f32_e32 v14, v14, v15
	v_fmamk_f32 v14, v14, 0x3c000000, v249
	v_rsq_f32_e32 v14, v14
	s_nop 0
	v_pk_mul_f32 v[12:13], v[14:15], v[12:13] op_sel_hi:[0,1]
	v_pk_mul_f32 v[10:11], v[222:223], v[12:13]
	s_nop 0
	v_cvt_pk_bf16_f32 v10, v10, v11
	global_store_dword v[8:9], v10, off
	v_lshl_add_u64 v[8:9], v[8:9], 0, s[6:7]
	s_branch .LBB0_575
.Lkx_orig:
.LBB0_574:
	s_ashr_i32 s6, s4, 13
	s_ashr_i32 s7, s6, 31
	s_and_b32 s5, s2, 0x1ffc00
	s_lshl_b64 s[8:9], s[6:7], 22
	s_add_u32 s7, s0, s8
	s_addc_u32 s8, s1, s9
	s_lshl_b32 s5, s5, 1
	s_add_u32 s5, s7, s5
	s_addc_u32 s7, s8, 0
	s_and_b32 s8, s3, 0x180
	s_lshl_b32 s8, s8, 1
	s_add_u32 s8, s5, s8
	s_addc_u32 s9, s7, 0
	v_lshl_add_u64 v[8:9], s[8:9], 0, v[112:113]
	flat_load_dword v13, v[8:9]
	s_lshl_b32 s6, s6, 7
	s_ashr_i32 s7, s6, 31
	v_lshl_add_u64 v[10:11], s[6:7], 2, v[0:1]
	global_load_dwordx2 v[10:11], v[10:11], off
	s_add_i32 s4, s4, s76
	s_add_i32 s3, s3, s82
	s_add_i32 s2, s2, s89
	s_cmpk_lt_i32 s4, 0x4000
	s_waitcnt vmcnt(0) lgkmcnt(0)
	v_lshlrev_b32_e32 v12, 16, v13
	v_and_b32_e32 v13, 0xffff0000, v13
	v_pk_mul_f32 v[14:15], v[12:13], v[12:13]
	s_nop 0
	v_add_f32_e32 v14, v14, v15
	s_waitcnt lgkmcnt(0)
	s_nop 1
	v_add_f32_dpp v15, v14, v14 quad_perm:[1,0,3,2] row_mask:0xf bank_mask:0xf
	s_nop 1
	v_add_f32_dpp v14, v15, v15 quad_perm:[2,3,0,1] row_mask:0xf bank_mask:0xf
	s_nop 1
	v_add_f32_dpp v15, v14, v14 row_half_mirror row_mask:0xf bank_mask:0xf
	s_nop 1
	v_add_f32_dpp v14, v15, v15 row_mirror row_mask:0xf bank_mask:0xf
	v_mov_b32_e32 v15, v14
	s_nop 1
	v_permlane16_swap_b32_e32 v14, v15
	v_add_f32_e32 v14, v14, v15
	v_mov_b32_e32 v15, v14
	s_nop 1
	v_permlane32_swap_b32_e32 v14, v15
	v_add_f32_e32 v14, v14, v15
	s_waitcnt lgkmcnt(0)
	v_fmamk_f32 v14, v14, 0x3c000000, v249
	v_rsq_f32_e32 v14, v14
	s_nop 0
	v_pk_mul_f32 v[12:13], v[14:15], v[12:13] op_sel_hi:[0,1]
	v_pk_mul_f32 v[10:11], v[10:11], v[12:13]
	s_nop 0
	v_cvt_pk_bf16_f32 v10, v10, v11
	flat_store_dword v[8:9], v10
	s_cbranch_scc1 .LBB0_574
